# v8: scan y stores from two running per-lane addresses (no per-chunk address arithmetic); compiler chunk step kept
# speedup vs baseline: 1.0117x; 1.0117x over previous
.LBB0_1720:
	s_waitcnt vmcnt(0)
	s_barrier
	s_lshl_b32 s1, s83, 2
	s_add_i32 s1, s1, 0xc400
	v_cmp_eq_u32_e32 vcc, 0, v0
	v_mov_b32_e32 v18, s1
	v_mov_b32_e32 v19, 0x104
	s_and_saveexec_b64 s[0:1], vcc
	s_cbranch_execz .Lx14_fin_skip
	global_store_dword v18, v19, s[54:55] sc1
.Lx14_fin_skip:
	s_or_b64 exec, exec, s[0:1]
	s_add_i32 s83, s83, s33
	s_cmpk_lt_i32 s83, 0x80
	s_waitcnt vmcnt(0) lgkmcnt(0)
	s_barrier
	s_cbranch_scc0 .LBB0_1770
.LBB0_1721:
	s_and_b32 s56, s83, 31
	s_bfe_u32 s73, s83, 0x10005
	s_lshl_b32 s72, s56, 6
	s_cmp_lt_u32 s83, 64
	s_cselect_b64 s[28:29], -1, 0
	s_and_b64 s[66:67], s[28:29], exec
	s_mov_b32 s0, 0x8c00000
	s_cselect_b32 s0, s0, 0x29400000
	s_add_u32 s66, s54, s0
	s_addc_u32 s67, s55, 0
	s_andn2_b64 vcc, exec, s[50:51]
	s_mov_b64 s[68:69], -1
	s_cbranch_vccnz .LBB0_1737
	s_and_saveexec_b64 s[68:69], s[4:5]
	v_mov_b32_e32 v2, s61
	ds_write_b32 v2, v161
	s_or_b64 exec, exec, s[68:69]
	s_lshl_b32 s0, s72, 1
	s_add_u32 s0, s66, s0
	s_addc_u32 s1, s67, 0
	s_add_u32 s0, s0, s81
	s_addc_u32 s1, s1, 0
	v_lshlrev_b32_e32 v160, 1, v158
	v_mov_b32_e32 v2, 0
	v_lshl_add_u64 v[164:165], s[0:1], 0, v[160:161]
	s_lshl_b32 s70, s73, 14
	s_mov_b32 s71, 0
	v_mov_b32_e32 v3, v2
	v_mov_b32_e32 v4, v2
	v_mov_b32_e32 v5, v2
	v_mov_b32_e32 v10, v2
	v_mov_b32_e32 v11, v2
	v_mov_b32_e32 v12, v2
	v_mov_b32_e32 v13, v2
	v_mov_b32_e32 v6, v2
	v_mov_b32_e32 v7, v2
	v_mov_b32_e32 v8, v2
	v_mov_b32_e32 v9, v2
	v_mov_b32_e32 v14, v2
	v_mov_b32_e32 v15, v2
	v_mov_b32_e32 v16, v2
	v_mov_b32_e32 v17, v2
	v_and_b32_e32 v25, 1, v0
	v_cmp_ne_u32_e64 s[98:99], 0, v25
	v_add_u32_e32 v24, v184, v25
	v_add_u32_e32 v22, 0xffffff00, v24
	v_sub_u32_e32 v23, 0x40ff, v24
	v_cndmask_b32_e64 v22, v23, v22, s[28:29]
	v_add_u32_e32 v22, s70, v22
	v_ashrrev_i32_e32 v23, 31, v22
	v_lshlrev_b64 v[22:23], 12, v[22:23]
	v_lshl_add_u64 v[22:23], v[164:165], 0, v[22:23]
	v_sub_u32_e32 v27, 0, v25
	v_lshlrev_b32_e32 v26, 1, v27
	v_lshl_add_u64 v[210:211], v[22:23], 0, v[26:27]
	v_mov_b32_e32 v28, 0x2000
	v_mov_b32_e32 v29, 0xffffe000
	v_cndmask_b32_e64 v28, v29, v28, s[28:29]
	v_ashrrev_i32_e32 v29, 31, v28
	v_lshl_add_u64 v[212:213], v[210:211], 0, v[28:29]
	s_mov_b32 s100, 0x10000
	s_mov_b32 s101, 0
	s_cmp_lt_u32 s83, 64
	s_cbranch_scc1 .Lx14_dir0
	s_mov_b32 s100, 0xffff0000
	s_mov_b32 s101, -1
.Lx14_dir0:
	s_waitcnt vmcnt(0) lgkmcnt(0)
	s_barrier
	s_branch .LBB0_1726

.LBB0_1726:
	s_add_i32 s0, s71, -1
	s_lshl_b32 s1, s83, 2
	s_add_i32 s1, s1, 0xc400
	v_cmp_eq_u32_e32 vcc, 0, v0
	v_mov_b32_e32 v18, s1
	v_mov_b32_e32 v19, s0
	s_and_saveexec_b64 s[0:1], vcc
	s_cbranch_execz .Lx14_pub_skip
	global_store_dword v18, v19, s[54:55] sc1
.Lx14_pub_skip:
	s_or_b64 exec, exec, s[0:1]
	s_and_b32 s0, s71, 1
	s_lshl_b32 s1, s0, 13
	s_add_i32 s1, s62, s1
	v_add_u32_e32 v18, s1, v159
	v_add_u32_e32 v18, 0x400, v18
	v_mov_b32_e32 v22, s1
	ds_read2_b32 v[180:181], v18 offset1:16
	ds_read2_b32 v[178:179], v18 offset0:32 offset1:48
	ds_read2_b32 v[176:177], v18 offset0:64 offset1:80
	ds_read2_b32 v[174:175], v18 offset0:96 offset1:112
	ds_read2_b32 v[172:173], v18 offset0:128 offset1:144
	ds_read2_b32 v[170:171], v18 offset0:160 offset1:176
	ds_read2_b32 v[168:169], v18 offset0:192 offset1:208
	ds_read2_b32 v[166:167], v18 offset0:224 offset1:240
	ds_read_b128 v[152:155], v22 offset:64
	ds_read_b128 v[148:151], v22 offset:128
	ds_read_b128 v[144:147], v22 offset:192
	ds_read_b128 v[140:143], v22 offset:256
	ds_read_b128 v[136:139], v22 offset:320
	ds_read_b128 v[132:135], v22 offset:336
	ds_read_b128 v[124:127], v22 offset:384
	ds_read_b128 v[120:123], v22 offset:400
	ds_read_b128 v[116:119], v22 offset:448
	ds_read_b128 v[112:115], v22 offset:464
	ds_read_b128 v[108:111], v22 offset:512
	ds_read_b128 v[104:107], v22 offset:528
	ds_read_b128 v[100:103], v22 offset:576
	ds_read_b128 v[96:99], v22 offset:592
	ds_read_b128 v[92:95], v22 offset:608
	ds_read_b128 v[88:91], v22 offset:640
	ds_read_b128 v[84:87], v22 offset:656
	ds_read_b128 v[80:83], v22 offset:672
	ds_read_b128 v[72:75], v22 offset:704
	ds_read_b128 v[68:71], v22 offset:720
	ds_read_b128 v[64:67], v22 offset:736
	ds_read_b128 v[60:63], v22 offset:768
	ds_read_b128 v[56:59], v22 offset:784
	ds_read_b128 v[52:55], v22 offset:800
	ds_read_b128 v[48:51], v22 offset:832
	ds_read_b128 v[44:47], v22 offset:848
	ds_read_b128 v[40:43], v22 offset:864
	ds_read_b128 v[36:39], v22 offset:880
	ds_read_b128 v[32:35], v22 offset:896
	ds_read_b128 v[28:31], v22 offset:912
	ds_read_b128 v[24:27], v22 offset:928
	ds_read_b128 v[18:21], v22 offset:944
	s_waitcnt lgkmcnt(14)
	ds_read_b128 v[154:157], v22 offset:960
	ds_read_b128 v[128:131], v22 offset:976
	ds_read_b128 v[76:79], v22 offset:992
	s_waitcnt lgkmcnt(3)
	ds_read_b128 v[20:23], v22 offset:1008
	s_waitcnt lgkmcnt(0)
	s_mul_i32 s0, s0, 0xcc00
	s_add_i32 s74, s0, 0
	s_and_saveexec_b64 s[68:69], s[8:9]
	s_cbranch_execz .LBB0_1728
	s_waitcnt lgkmcnt(0)
	v_cndmask_b32_e64 v23, v167, v250, s[6:7]
	v_cndmask_b32_e64 v37, v180, v251, s[6:7]
	v_cndmask_b32_e64 v38, v181, v252, s[6:7]
	v_cndmask_b32_e64 v39, v178, v253, s[6:7]
	v_cndmask_b32_e64 v67, v179, v254, s[6:7]
	v_cndmask_b32_e64 v82, v176, v189, s[6:7]
	v_cndmask_b32_e64 v83, v177, v195, s[6:7]
	v_cndmask_b32_e64 v93, v174, v196, s[6:7]
	v_cndmask_b32_e64 v94, v175, v197, s[6:7]
	v_cndmask_b32_e64 v95, v172, v200, s[6:7]
	v_fmac_f32_e32 v23, v37, v154
	v_fmac_f32_e32 v38, v37, v152
	v_fmac_f32_e32 v39, v37, v148
	v_fmac_f32_e32 v67, v37, v144
	v_fmac_f32_e32 v82, v37, v140
	v_fmac_f32_e32 v83, v37, v136
	v_fmac_f32_e32 v93, v37, v124
	v_fmac_f32_e32 v94, v37, v116
	v_fmac_f32_e32 v95, v37, v108
	v_fmac_f32_e32 v23, v38, v155
	v_fmac_f32_e32 v39, v149, v38
	v_fmac_f32_e32 v67, v38, v145
	v_fmac_f32_e32 v82, v38, v141
	v_fmac_f32_e32 v83, v38, v137
	v_fmac_f32_e32 v93, v38, v125
	v_fmac_f32_e32 v94, v38, v117
	v_fmac_f32_e32 v95, v38, v109
	v_fmac_f32_e32 v23, v39, v156
	v_fmac_f32_e32 v67, v146, v39
	v_fmac_f32_e32 v82, v142, v39
	v_fmac_f32_e32 v83, v39, v138
	v_fmac_f32_e32 v93, v39, v126
	v_fmac_f32_e32 v94, v39, v118
	v_fmac_f32_e32 v95, v39, v110
	v_fmac_f32_e32 v23, v67, v157
	v_fmac_f32_e32 v82, v143, v67
	v_fmac_f32_e32 v83, v139, v67
	v_fmac_f32_e32 v93, v67, v127
	v_fmac_f32_e32 v94, v67, v119
	v_fmac_f32_e32 v95, v67, v111
	v_fmac_f32_e32 v23, v82, v128
	v_fmac_f32_e32 v83, v132, v82
	v_fmac_f32_e32 v93, v120, v82
	v_fmac_f32_e32 v94, v82, v112
	v_fmac_f32_e32 v95, v82, v104
	v_fmac_f32_e32 v23, v83, v129
	v_fmac_f32_e32 v93, v121, v83
	v_fmac_f32_e32 v94, v113, v83
	v_fmac_f32_e32 v95, v83, v105
	v_fmac_f32_e32 v23, v93, v130
	v_fmac_f32_e32 v94, v114, v93
	v_fmac_f32_e32 v95, v106, v93
	v_fmac_f32_e32 v23, v94, v131
	v_fmac_f32_e32 v95, v107, v94
	v_fmac_f32_e32 v23, v95, v76
	v_cndmask_b32_e64 v76, v173, v201, s[6:7]
	v_fmac_f32_e32 v76, v37, v100
	v_fmac_f32_e32 v76, v38, v101
	v_fmac_f32_e32 v76, v39, v102
	v_fmac_f32_e32 v76, v67, v103
	v_fmac_f32_e32 v76, v82, v96
	v_fmac_f32_e32 v76, v83, v97
	v_fmac_f32_e32 v76, v93, v98
	v_fmac_f32_e32 v76, v99, v94
	v_fmac_f32_e32 v76, v92, v95
	v_fmac_f32_e32 v23, v76, v77
	v_cndmask_b32_e64 v77, v170, v202, s[6:7]
	v_fmac_f32_e32 v77, v37, v88
	v_fmac_f32_e32 v77, v38, v89
	v_fmac_f32_e32 v77, v39, v90
	v_fmac_f32_e32 v77, v67, v91
	v_fmac_f32_e32 v77, v82, v84
	v_fmac_f32_e32 v77, v83, v85
	v_fmac_f32_e32 v77, v93, v86
	v_fmac_f32_e32 v77, v94, v87
	v_fmac_f32_e32 v77, v80, v95
	v_fmac_f32_e32 v77, v81, v76
	v_fmac_f32_e32 v23, v77, v78
	v_cndmask_b32_e64 v78, v171, v204, s[6:7]
	v_fmac_f32_e32 v78, v37, v72
	v_fmac_f32_e32 v78, v38, v73
	v_fmac_f32_e32 v78, v39, v74
	v_fmac_f32_e32 v78, v67, v75
	v_fmac_f32_e32 v78, v82, v68
	v_fmac_f32_e32 v78, v83, v69
	v_fmac_f32_e32 v78, v93, v70
	v_fmac_f32_e32 v78, v94, v71
	v_fmac_f32_e32 v78, v95, v64
	v_cndmask_b32_e64 v64, v168, v205, s[6:7]
	v_fmac_f32_e32 v64, v37, v60
	v_fmac_f32_e32 v64, v38, v61
	v_fmac_f32_e32 v64, v39, v62
	v_fmac_f32_e32 v64, v67, v63
	v_fmac_f32_e32 v64, v82, v56
	v_fmac_f32_e32 v64, v83, v57
	v_fmac_f32_e32 v64, v93, v58
	v_fmac_f32_e32 v64, v94, v59
	v_fmac_f32_e32 v64, v95, v52
	v_fmac_f32_e32 v78, v65, v76
	v_fmac_f32_e32 v64, v76, v53
	v_fmac_f32_e32 v78, v66, v77
	v_fmac_f32_e32 v64, v54, v77
	v_fmac_f32_e32 v23, v78, v79
	v_fmac_f32_e32 v64, v55, v78
	v_fmac_f32_e32 v23, v64, v20
	v_cndmask_b32_e64 v20, v169, v206, s[6:7]
	v_fmac_f32_e32 v20, v37, v48
	v_fmac_f32_e32 v20, v38, v49
	v_fmac_f32_e32 v20, v39, v50
	v_fmac_f32_e32 v20, v67, v51
	v_fmac_f32_e32 v20, v82, v44
	v_fmac_f32_e32 v20, v83, v45
	v_fmac_f32_e32 v20, v93, v46
	v_fmac_f32_e32 v20, v94, v47
	v_fmac_f32_e32 v20, v95, v40
	v_fmac_f32_e32 v20, v76, v41
	v_fmac_f32_e32 v20, v77, v42
	v_fmac_f32_e32 v20, v43, v78
	v_fmac_f32_e32 v20, v36, v64
	v_fmac_f32_e32 v23, v21, v20
	v_cndmask_b32_e64 v21, v166, v209, s[6:7]
	v_fmac_f32_e32 v21, v37, v32
	v_fmac_f32_e32 v21, v38, v33
	v_fmac_f32_e32 v21, v39, v34
	v_fmac_f32_e32 v21, v67, v35
	v_fmac_f32_e32 v21, v82, v28
	v_fmac_f32_e32 v21, v83, v29
	v_fmac_f32_e32 v21, v93, v30
	v_fmac_f32_e32 v21, v94, v31
	v_fmac_f32_e32 v21, v95, v24
	v_fmac_f32_e32 v21, v76, v25
	v_fmac_f32_e32 v21, v77, v26
	s_mul_i32 s0, s82, 0x3300
	v_fmac_f32_e32 v21, v78, v27
	s_add_i32 s0, s74, s0
	v_fmac_f32_e32 v21, v18, v64
	v_add_u32_e32 v18, s0, v163
	v_fmac_f32_e32 v21, v19, v20
	v_add3_u32 v18, v18, v182, v183
	v_cvt_pk_bf16_f32 v19, v37, s0
	ds_write_b16 v18, v19 offset:8704
	v_cvt_pk_bf16_f32 v19, v38, s0
	ds_write_b16 v18, v19 offset:8768
	v_cvt_pk_bf16_f32 v19, v39, s0
	ds_write_b16 v18, v19 offset:8832
	v_cvt_pk_bf16_f32 v19, v67, s0
	ds_write_b16 v18, v19 offset:8896
	v_cvt_pk_bf16_f32 v19, v82, s0
	ds_write_b16 v18, v19 offset:8960
	v_cvt_pk_bf16_f32 v19, v83, s0
	ds_write_b16 v18, v19 offset:9024
	v_cvt_pk_bf16_f32 v19, v93, s0
	ds_write_b16 v18, v19 offset:9088
	v_cvt_pk_bf16_f32 v19, v94, s0
	ds_write_b16 v18, v19 offset:9152
	v_cvt_pk_bf16_f32 v19, v95, s0
	ds_write_b16 v18, v19 offset:9216
	v_cvt_pk_bf16_f32 v19, v76, s0
	ds_write_b16 v18, v19 offset:9280
	v_cvt_pk_bf16_f32 v19, v77, s0
	ds_write_b16 v18, v19 offset:9344
	v_cvt_pk_bf16_f32 v19, v78, s0
	ds_write_b16 v18, v19 offset:9408
	v_cvt_pk_bf16_f32 v19, v64, s0
	ds_write_b16 v18, v19 offset:9472
	v_cvt_pk_bf16_f32 v19, v20, s0
	v_fmac_f32_e32 v23, v22, v21
	ds_write_b16 v18, v19 offset:9536
	v_cvt_pk_bf16_f32 v19, v21, s0
	ds_write_b16 v18, v19 offset:9600
	v_cvt_pk_bf16_f32 v19, v23, s0
	ds_write_b16 v18, v19 offset:9664

.LBB0_1731:
	v_lshl_add_u64 v[210:211], v[210:211], 0, s[100:101]
	v_lshl_add_u64 v[212:213], v[212:213], 0, s[100:101]
	s_add_i32 s69, s69, 1
	s_cmp_eq_u32 s69, 4
	s_cbranch_scc1 .LBB0_1725

.LBB0_1734:
	s_mul_i32 s0, s69, 0x3300
	s_add_i32 s0, s74, s0
	s_add_i32 s1, s0, 0x2a00
	v_add_u32_e32 v18, s1, v185
	ds_read_b64_tr_b16 v[20:21], v18
	v_add3_u32 v18, s0, v186, v187
	ds_read2_b64 v[26:29], v18 offset1:4
	ds_read2_b64 v[30:33], v18 offset0:8 offset1:12
	v_add_u32_e32 v18, 0x800, v18
	v_cvt_pk_bf16_f32 v22, v2, v3
	v_cvt_pk_bf16_f32 v23, v4, v5
	v_cvt_pk_bf16_f32 v24, v10, v11
	v_cvt_pk_bf16_f32 v25, v12, v13
	ds_read2_b64 v[38:41], v18 offset0:32 offset1:36
	ds_read2_b64 v[42:45], v18 offset0:40 offset1:44
	s_waitcnt lgkmcnt(3)
	v_mfma_f32_16x16x32_bf16 v[26:29], v[26:29], v[22:25], 0
	s_waitcnt lgkmcnt(0)
	s_add_i32 s76, s69, s68
	v_cvt_pk_bf16_f32 v34, v6, v7
	v_cvt_pk_bf16_f32 v35, v8, v9
	v_cvt_pk_bf16_f32 v36, v14, v15
	v_cvt_pk_bf16_f32 v37, v16, v17
	s_waitcnt lgkmcnt(2)
	s_nop 0
	v_mfma_f32_16x16x32_bf16 v[26:29], v[30:33], v[34:37], v[26:29]
	s_nop 7
	v_cvt_pk_bf16_f32 v18, v26, v27
	v_add_u32_e32 v26, s0, v192
	ds_read_b128 v[30:33], v26 offset:8704
	v_add_u32_e32 v62, s0, v191
	ds_read_b128 v[46:49], v62 offset:12800
	v_cvt_pk_bf16_f32 v19, v28, v29
	ds_read_b128 v[26:29], v26 offset:9728
	ds_read_b128 v[50:53], v62 offset:12864
	v_add_u32_e32 v63, v62, v190
	ds_read_b128 v[54:57], v63 offset:4608
	ds_read_b128 v[58:61], v63 offset:5632
	s_waitcnt lgkmcnt(5)
	v_mfma_f32_16x16x32_bf16 v[30:33], v[30:33], v[18:21], 0
	s_waitcnt lgkmcnt(2)
	v_pk_mul_f32 v[10:11], v[10:11], v[50:51]
	v_pk_mul_f32 v[12:13], v[12:13], v[52:53]
	ds_read_b128 v[50:53], v63 offset:7680
	v_mfma_f32_16x16x32_bf16 v[22:25], v[38:41], v[22:25], 0
	s_nop 2
	v_cvt_pk_bf16_f32 v18, v30, v31
	v_cvt_pk_bf16_f32 v19, v32, v33
	ds_read_b128 v[30:33], v63 offset:6656
	v_pk_mul_f32 v[2:3], v[2:3], v[46:47]
	v_pk_mul_f32 v[4:5], v[4:5], v[48:49]
	ds_read_b128 v[46:49], v62 offset:12928
	v_mfma_f32_16x16x32_bf16 v[22:25], v[42:45], v[34:37], v[22:25]
	s_cmp_lt_u32 s76, 16
	s_waitcnt lgkmcnt(4)
	v_mfma_f32_16x16x32_bf16 v[2:5], v[54:57], v[18:21], v[2:5]
	ds_read_b128 v[54:57], v62 offset:12992
	s_waitcnt lgkmcnt(1)
	v_pk_mul_f32 v[6:7], v[6:7], v[46:47]
	v_pk_mul_f32 v[8:9], v[8:9], v[48:49]
	v_mfma_f32_16x16x32_bf16 v[10:13], v[58:61], v[18:21], v[10:13]
	s_waitcnt lgkmcnt(0)
	v_pk_mul_f32 v[14:15], v[14:15], v[54:55]
	v_pk_mul_f32 v[16:17], v[16:17], v[56:57]
	v_mfma_f32_16x16x32_bf16 v[6:9], v[30:33], v[18:21], v[6:9]
	s_nop 0
	v_mfma_f32_16x16x32_bf16 v[14:17], v[50:53], v[18:21], v[14:17]
	v_mfma_f32_16x16x32_bf16 v[18:21], v[26:29], v[18:21], v[22:25]
	s_cbranch_scc1 .LBB0_1731
	s_nop 6
	v_mov_b32_dpp v32, v18 quad_perm:[1,0,3,2] row_mask:0xf bank_mask:0xf bound_ctrl:1
	v_mov_b32_dpp v33, v19 quad_perm:[1,0,3,2] row_mask:0xf bank_mask:0xf bound_ctrl:1
	v_mov_b32_dpp v34, v20 quad_perm:[1,0,3,2] row_mask:0xf bank_mask:0xf bound_ctrl:1
	v_mov_b32_dpp v35, v21 quad_perm:[1,0,3,2] row_mask:0xf bank_mask:0xf bound_ctrl:1
	v_cndmask_b32_e64 v36, v18, v33, s[98:99]
	v_cndmask_b32_e64 v37, v32, v19, s[98:99]
	v_cndmask_b32_e64 v38, v20, v35, s[98:99]
	v_cndmask_b32_e64 v39, v34, v21, s[98:99]
	v_cvt_pk_bf16_f32 v36, v36, v37
	v_cvt_pk_bf16_f32 v38, v38, v39
	global_store_dword v[210:211], v36, off sc1
	global_store_dword v[212:213], v38, off sc1
	s_branch .LBB0_1731
